# v21 + one s_nop at entry (code placement)
# speedup vs baseline: 1.0077x; 1.0077x over previous
_Z6mk_fwd4Args:
	s_nop 0
	s_load_dword s96, s[0:1], 0xa8
	s_load_dwordx8 s[52:59], s[0:1], 0x80
	s_load_dwordx16 s[60:75], s[0:1], 0x0
	s_load_dwordx16 s[36:51], s[0:1], 0x40
	v_writelane_b32 v254, s2, 0
	v_lshlrev_b32_e32 v244, 2, v0
	v_add_u32_e32 v1, 0, v244
	v_writelane_b32 v254, s3, 1
	v_readfirstlane_b32 s2, v0
	v_add_u32_e32 v1, 0x21800, v1
	s_mov_b64 s[4:5], 0
	v_writelane_b32 v254, s2, 2
	s_add_u32 s2, s0, 0xa8
	s_addc_u32 s3, s1, 0
	v_writelane_b32 v254, s2, 3
	v_mov_b32_e32 v2, 0
	s_nop 0
	v_writelane_b32 v254, s3, 4
	s_mov_b32 s2, 0
	s_mov_b32 s3, 1
	s_mov_b32 s6, s2
	s_branch .LBB0_2
